# step-3 unit: gate loads, row-piece loads and epilogue norm-weight loads batched; hyena latent unit tap weights loaded once
# speedup vs baseline: 1.0013x; 1.0013x over previous
.LBB0_669:
	s_or_b64 exec, exec, s[10:11]
	s_add_i32 s100, s46, 0x0
	s_lshl_b32 s100, s100, 2
	v_mov_b32_e32 v108, s100
	global_load_dword v90, v108, s[4:5]
	s_add_i32 s100, s46, 0x600
	s_lshl_b32 s100, s100, 2
	v_mov_b32_e32 v108, s100
	global_load_dword v92, v108, s[4:5]
	s_add_i32 s100, s46, 0xc00
	s_lshl_b32 s100, s100, 2
	v_mov_b32_e32 v108, s100
	global_load_dword v94, v108, s[4:5]
	s_add_i32 s100, s46, 0x200
	s_lshl_b32 s100, s100, 2
	v_mov_b32_e32 v108, s100
	global_load_dword v96, v108, s[4:5]
	s_add_i32 s100, s46, 0x800
	s_lshl_b32 s100, s100, 2
	v_mov_b32_e32 v108, s100
	global_load_dword v98, v108, s[4:5]
	s_add_i32 s100, s46, 0xe00
	s_lshl_b32 s100, s100, 2
	v_mov_b32_e32 v108, s100
	global_load_dword v100, v108, s[4:5]
	s_add_i32 s100, s46, 0x400
	s_lshl_b32 s100, s100, 2
	v_mov_b32_e32 v108, s100
	global_load_dword v102, v108, s[4:5]
	s_add_i32 s100, s46, 0xa00
	s_lshl_b32 s100, s100, 2
	v_mov_b32_e32 v108, s100
	global_load_dword v104, v108, s[4:5]
	s_add_i32 s100, s46, 0x1000
	s_lshl_b32 s100, s100, 2
	v_mov_b32_e32 v108, s100
	global_load_dword v106, v108, s[4:5]
	v_ashrrev_i32_e32 v56, 10, v1
	v_lshlrev_b32_e32 v36, 9, v56
	v_add_u32_e32 v62, s46, v36
	v_ashrrev_i32_e32 v63, 31, v62
	s_add_i32 s11, s46, 0x600
	v_lshl_add_u64 v[62:63], v[62:63], 2, s[4:5]
	global_load_dword v2, v[62:63], off
	v_add_u32_e32 v62, s11, v36
	v_ashrrev_i32_e32 v63, 31, v62
	s_add_i32 s10, s46, 0xc00
	v_lshl_add_u64 v[62:63], v[62:63], 2, s[4:5]
	global_load_dword v32, v[62:63], off
	v_add_u32_e32 v62, s10, v36
	v_ashrrev_i32_e32 v63, 31, v62
	v_lshl_add_u64 v[62:63], v[62:63], 2, s[4:5]
	global_load_dword v36, v[62:63], off
	s_waitcnt vmcnt(3)
	v_lshlrev_b32_e32 v54, 16, v54
	v_lshlrev_b32_e32 v53, 16, v53
	v_lshlrev_b32_e32 v50, 16, v50
	v_lshlrev_b32_e32 v49, 16, v49
	v_lshlrev_b32_e32 v46, 16, v46
	v_lshlrev_b32_e32 v45, 16, v45
	v_lshlrev_b32_e32 v42, 16, v42
	v_lshlrev_b32_e32 v41, 16, v41
	v_lshlrev_b32_e32 v38, 16, v38
	v_lshlrev_b32_e32 v37, 16, v37
	v_lshlrev_b32_e32 v34, 16, v34
	v_lshlrev_b32_e32 v33, 16, v33
	v_bfe_u32 v62, v1, 9, 1
	v_cmp_lt_u32_e32 vcc, s23, v1
	s_and_saveexec_b64 s[0:1], vcc
	s_xor_b64 s[0:1], exec, s[0:1]
	s_cbranch_execz .LBB0_671
	s_mov_b64 s[38:39], src_shared_base
	s_cmp_lg_u32 0, -1
	s_cselect_b32 s38, 0, 0
	s_cselect_b32 s39, s39, 0
	s_add_u32 s38, s38, 0x1a1a0
	s_addc_u32 s39, s39, 0
	s_cmp_lg_u64 s[38:39], 0
	s_cselect_b32 s38, s38, -1
	s_add_i32 s39, 0, 0x1e1a0
	v_mov_b32_e32 v40, s39
	v_mov_b32_e32 v43, s38
	v_cmp_eq_u32_e32 vcc, 1, v56
	s_nop 1
	v_cndmask_b32_e32 v40, v40, v43, vcc
	v_lshl_add_u32 v40, v62, 13, v40
.LBB0_671:
	s_or_saveexec_b64 s[0:1], s[0:1]
	v_lshrrev_b32_e32 v43, 1, v28
	v_and_b32_e32 v43, 0x7f0, v43
	v_readlane_b32 s20, v249, 37
	s_nop 1
	v_add_u32_e32 v57, s20, v43
	v_mad_u32_u24 v63, v62, s24, v57
	s_xor_b64 exec, exec, s[0:1]
	v_mad_u32_u24 v40, v62, s24, v57
	s_or_b64 exec, exec, s[0:1]
	s_waitcnt vmcnt(8)
	v_lshlrev_b32_e32 v55, 16, v24
	v_and_b32_e32 v72, 0xffff0000, v24
	v_and_b32_e32 v70, 0xffff0000, v25
	v_lshlrev_b32_e32 v73, 16, v25
	v_mov_b32_e32 v24, v55
	v_mov_b32_e32 v25, v72
	v_and_b32_e32 v71, 16, v26
	s_waitcnt vmcnt(1)
	v_pk_mul_f32 v[24:25], v[32:33], v[24:25] op_sel_hi:[0,1]
	v_pk_fma_f32 v[24:25], v[54:55], v[2:3], v[24:25] op_sel_hi:[1,0,1]
	v_pk_mov_b32 v[54:55], v[72:73], v[70:71] op_sel:[1,0]
	v_and_b32_e32 v65, 0xffff0000, v27
	v_pk_mul_f32 v[54:55], v[32:33], v[54:55] op_sel_hi:[0,1]
	v_and_b32_e32 v67, 16, v27
	v_and_b32_e32 v66, 0xffff0000, v26
	v_lshlrev_b32_e32 v69, 16, v27
	v_lshlrev_b32_e32 v27, 16, v26
	v_mov_b32_e32 v26, v70
	v_pk_fma_f32 v[54:55], v[2:3], v[72:73], v[54:55] op_sel_hi:[0,1,1]
	s_waitcnt vmcnt(0)
	v_pk_fma_f32 v[24:25], v[36:37], v[72:73], v[24:25] op_sel_hi:[0,1,1]
	v_pk_fma_f32 v[54:55], v[36:37], v[26:27], v[54:55] op_sel_hi:[0,1,1]
	v_cvt_pk_bf16_f32 v24, v24, v25
	v_cvt_pk_bf16_f32 v25, v54, v55
	v_pk_mov_b32 v[54:55], v[26:27], v[66:67] op_sel:[1,0]
	v_mov_b32_e32 v64, v69
	v_pk_mul_f32 v[54:55], v[32:33], v[54:55] op_sel_hi:[0,1]
	v_mov_b32_e32 v68, v66
	v_pk_fma_f32 v[26:27], v[2:3], v[26:27], v[54:55] op_sel_hi:[0,1,1]
	v_pk_mul_f32 v[54:55], v[32:33], v[64:65] op_sel_hi:[0,1]
	v_pk_fma_f32 v[54:55], v[2:3], v[68:69], v[54:55] op_sel_hi:[0,1,1]
	v_mov_b32_e32 v52, v65
	v_pk_fma_f32 v[26:27], v[36:37], v[68:69], v[26:27] op_sel_hi:[0,1,1]
	v_pk_fma_f32 v[52:53], v[36:37], v[52:53], v[54:55] op_sel_hi:[0,1,1]
	v_cvt_pk_bf16_f32 v26, v26, v27
	v_cvt_pk_bf16_f32 v27, v52, v53
	v_lshl_add_u32 v2, v59, 1, v40
	ds_write_b128 v2, v[24:27]
	v_ashrrev_i32_e32 v25, 10, v58
	v_lshlrev_b32_e32 v32, 9, v25
	v_add_u32_e32 v26, s46, v32
	v_ashrrev_i32_e32 v27, 31, v26
	v_lshl_add_u64 v[26:27], v[26:27], 2, s[4:5]
	v_add_u32_e32 v26, s11, v32
	v_ashrrev_i32_e32 v27, 31, v26
	v_lshl_add_u64 v[26:27], v[26:27], 2, s[4:5]
	v_add_u32_e32 v26, s10, v32
	v_ashrrev_i32_e32 v27, 31, v26
	v_lshl_add_u64 v[26:27], v[26:27], 2, s[4:5]
	v_bfe_u32 v32, v58, 9, 1
	v_cmp_lt_u32_e32 vcc, s23, v58
	s_and_saveexec_b64 s[0:1], vcc
	s_xor_b64 s[0:1], exec, s[0:1]
	s_cbranch_execz .LBB0_675
	s_mov_b64 s[38:39], src_shared_base
	s_cmp_lg_u32 0, -1
	s_cselect_b32 s38, 0, 0
	s_cselect_b32 s39, s39, 0
	s_add_u32 s38, s38, 0x1a1a0
	s_addc_u32 s39, s39, 0
	s_cmp_lg_u64 s[38:39], 0
	s_cselect_b32 s38, s38, -1
	s_add_i32 s39, 0, 0x1e1a0
	v_mov_b32_e32 v27, s39
	v_mov_b32_e32 v36, s38
	v_cmp_eq_u32_e32 vcc, 1, v25
	s_nop 1
	v_cndmask_b32_e32 v27, v27, v36, vcc
	v_lshl_add_u32 v27, v32, 13, v27
.LBB0_675:
	s_andn2_saveexec_b64 s[0:1], s[0:1]
	v_mad_u32_u24 v27, v32, s24, v57
	s_or_b64 exec, exec, s[0:1]
	v_lshlrev_b32_e32 v51, 16, v20
	v_and_b32_e32 v68, 0xffff0000, v20
	v_and_b32_e32 v66, 0xffff0000, v21
	v_lshlrev_b32_e32 v69, 16, v21
	v_mov_b32_e32 v20, v51
	v_mov_b32_e32 v21, v68
	v_and_b32_e32 v67, 16, v22
	s_waitcnt vmcnt(1)
	v_pk_mul_f32 v[20:21], v[92:93], v[20:21] op_sel_hi:[0,1]
	v_pk_fma_f32 v[20:21], v[50:51], v[90:91], v[20:21] op_sel_hi:[1,0,1]
	v_pk_mov_b32 v[50:51], v[68:69], v[66:67] op_sel:[1,0]
	v_and_b32_e32 v53, 0xffff0000, v23
	v_pk_mul_f32 v[50:51], v[92:93], v[50:51] op_sel_hi:[0,1]
	v_and_b32_e32 v55, 16, v23
	v_and_b32_e32 v54, 0xffff0000, v22
	v_lshlrev_b32_e32 v65, 16, v23
	v_lshlrev_b32_e32 v23, 16, v22
	v_mov_b32_e32 v22, v66
	v_pk_fma_f32 v[50:51], v[90:91], v[68:69], v[50:51] op_sel_hi:[0,1,1]
	s_waitcnt vmcnt(0)
	v_pk_fma_f32 v[20:21], v[94:95], v[68:69], v[20:21] op_sel_hi:[0,1,1]
	v_pk_fma_f32 v[50:51], v[94:95], v[22:23], v[50:51] op_sel_hi:[0,1,1]
	v_cvt_pk_bf16_f32 v20, v20, v21
	v_cvt_pk_bf16_f32 v21, v50, v51
	v_pk_mov_b32 v[50:51], v[22:23], v[54:55] op_sel:[1,0]
	v_mov_b32_e32 v52, v65
	v_pk_mul_f32 v[50:51], v[92:93], v[50:51] op_sel_hi:[0,1]
	v_mov_b32_e32 v64, v54
	v_pk_fma_f32 v[22:23], v[90:91], v[22:23], v[50:51] op_sel_hi:[0,1,1]
	v_pk_mul_f32 v[50:51], v[92:93], v[52:53] op_sel_hi:[0,1]
	v_pk_fma_f32 v[50:51], v[90:91], v[64:65], v[50:51] op_sel_hi:[0,1,1]
	v_mov_b32_e32 v48, v53
	v_pk_fma_f32 v[22:23], v[94:95], v[64:65], v[22:23] op_sel_hi:[0,1,1]
	v_pk_fma_f32 v[48:49], v[94:95], v[48:49], v[50:51] op_sel_hi:[0,1,1]
	v_cvt_pk_bf16_f32 v22, v22, v23
	v_cvt_pk_bf16_f32 v23, v48, v49
	v_lshl_add_u32 v2, v59, 1, v27
	ds_write_b128 v2, v[20:23]
	v_ashrrev_i32_e32 v21, 10, v60
	v_lshlrev_b32_e32 v24, 9, v21
	v_add_u32_e32 v22, s46, v24
	v_ashrrev_i32_e32 v23, 31, v22
	v_lshl_add_u64 v[22:23], v[22:23], 2, s[4:5]
	v_add_u32_e32 v22, s11, v24
	v_ashrrev_i32_e32 v23, 31, v22
	v_lshl_add_u64 v[22:23], v[22:23], 2, s[4:5]
	v_add_u32_e32 v22, s10, v24
	v_ashrrev_i32_e32 v23, 31, v22
	v_lshl_add_u64 v[22:23], v[22:23], 2, s[4:5]
	s_movk_i32 s0, 0xfc00
	v_cmp_gt_u32_e32 vcc, s0, v1
	s_and_saveexec_b64 s[0:1], vcc
	s_xor_b64 s[0:1], exec, s[0:1]
	s_cbranch_execz .LBB0_679
	s_mov_b64 s[38:39], src_shared_base
	s_cmp_lg_u32 0, -1
	s_cselect_b32 s38, 0, 0
	s_cselect_b32 s39, s39, 0
	s_add_u32 s38, s38, 0x1a1a0
	s_addc_u32 s39, s39, 0
	s_cmp_lg_u64 s[38:39], 0
	s_cselect_b32 s38, s38, -1
	s_add_i32 s39, 0, 0x1e1a0
	v_mov_b32_e32 v23, s39
	v_mov_b32_e32 v24, s38
	v_cmp_eq_u32_e32 vcc, 1, v21
	s_nop 1
	v_cndmask_b32_e32 v23, v23, v24, vcc
	v_lshl_add_u32 v23, v62, 13, v23
.LBB0_679:
	s_andn2_saveexec_b64 s[0:1], s[0:1]
	v_mad_u32_u24 v23, v62, s24, v57
	s_or_b64 exec, exec, s[0:1]
	v_lshlrev_b32_e32 v47, 16, v16
	v_and_b32_e32 v54, 0xffff0000, v16
	v_and_b32_e32 v52, 0xffff0000, v17
	v_lshlrev_b32_e32 v55, 16, v17
	v_mov_b32_e32 v16, v47
	v_mov_b32_e32 v17, v54
	v_and_b32_e32 v53, 16, v18
	s_waitcnt vmcnt(1)
	v_pk_mul_f32 v[16:17], v[98:99], v[16:17] op_sel_hi:[0,1]
	v_pk_fma_f32 v[16:17], v[46:47], v[96:97], v[16:17] op_sel_hi:[1,0,1]
	v_pk_mov_b32 v[46:47], v[54:55], v[52:53] op_sel:[1,0]
	v_and_b32_e32 v27, 0xffff0000, v19
	v_pk_mul_f32 v[46:47], v[98:99], v[46:47] op_sel_hi:[0,1]
	v_and_b32_e32 v49, 16, v19
	v_and_b32_e32 v48, 0xffff0000, v18
	v_lshlrev_b32_e32 v51, 16, v19
	v_lshlrev_b32_e32 v19, 16, v18
	v_mov_b32_e32 v18, v52
	v_pk_fma_f32 v[46:47], v[96:97], v[54:55], v[46:47] op_sel_hi:[0,1,1]
	s_waitcnt vmcnt(0)
	v_pk_fma_f32 v[16:17], v[100:101], v[54:55], v[16:17] op_sel_hi:[0,1,1]
	v_pk_fma_f32 v[46:47], v[100:101], v[18:19], v[46:47] op_sel_hi:[0,1,1]
	v_cvt_pk_bf16_f32 v16, v16, v17
	v_cvt_pk_bf16_f32 v17, v46, v47
	v_pk_mov_b32 v[46:47], v[18:19], v[48:49] op_sel:[1,0]
	v_mov_b32_e32 v26, v51
	v_pk_mul_f32 v[46:47], v[98:99], v[46:47] op_sel_hi:[0,1]
	v_mov_b32_e32 v50, v48
	v_pk_fma_f32 v[18:19], v[96:97], v[18:19], v[46:47] op_sel_hi:[0,1,1]
	v_pk_mul_f32 v[46:47], v[98:99], v[26:27] op_sel_hi:[0,1]
	v_pk_fma_f32 v[46:47], v[96:97], v[50:51], v[46:47] op_sel_hi:[0,1,1]
	v_mov_b32_e32 v44, v27
	v_pk_fma_f32 v[18:19], v[100:101], v[50:51], v[18:19] op_sel_hi:[0,1,1]
	v_pk_fma_f32 v[26:27], v[100:101], v[44:45], v[46:47] op_sel_hi:[0,1,1]
	v_cvt_pk_bf16_f32 v18, v18, v19
	v_cvt_pk_bf16_f32 v19, v26, v27
	v_lshl_add_u32 v2, v59, 1, v23
	ds_write_b128 v2, v[16:19]
	v_ashrrev_i32_e32 v17, 10, v61
	v_lshlrev_b32_e32 v20, 9, v17
	v_add_u32_e32 v18, s46, v20
	v_ashrrev_i32_e32 v19, 31, v18
	v_lshl_add_u64 v[18:19], v[18:19], 2, s[4:5]
	v_add_u32_e32 v18, s11, v20
	v_ashrrev_i32_e32 v19, 31, v18
	v_lshl_add_u64 v[18:19], v[18:19], 2, s[4:5]
	v_add_u32_e32 v18, s10, v20
	v_ashrrev_i32_e32 v19, 31, v18
	v_lshl_add_u64 v[18:19], v[18:19], 2, s[4:5]
	v_bfe_u32 v20, v61, 9, 1
	v_cmp_lt_u32_e32 vcc, s23, v61
	s_and_saveexec_b64 s[0:1], vcc
	s_xor_b64 s[0:1], exec, s[0:1]
	s_cbranch_execz .LBB0_683
	s_mov_b64 s[38:39], src_shared_base
	s_cmp_lg_u32 0, -1
	s_cselect_b32 s38, 0, 0
	s_cselect_b32 s39, s39, 0
	s_add_u32 s38, s38, 0x1a1a0
	s_addc_u32 s39, s39, 0
	s_cmp_lg_u64 s[38:39], 0
	s_cselect_b32 s38, s38, -1
	s_add_i32 s39, 0, 0x1e1a0
	v_mov_b32_e32 v19, s39
	v_mov_b32_e32 v22, s38
	v_cmp_eq_u32_e32 vcc, 1, v17
	s_nop 1
	v_cndmask_b32_e32 v19, v19, v22, vcc
	v_lshl_add_u32 v19, v20, 13, v19
.LBB0_683:
	s_andn2_saveexec_b64 s[0:1], s[0:1]
	v_mad_u32_u24 v19, v20, s24, v57
	s_or_b64 exec, exec, s[0:1]
	v_lshlrev_b32_e32 v43, 16, v12
	v_and_b32_e32 v48, 0xffff0000, v12
	v_and_b32_e32 v46, 0xffff0000, v13
	v_lshlrev_b32_e32 v49, 16, v13
	v_mov_b32_e32 v12, v43
	v_mov_b32_e32 v13, v48
	v_and_b32_e32 v47, 16, v14
	s_waitcnt vmcnt(1)
	v_pk_mul_f32 v[12:13], v[98:99], v[12:13] op_sel_hi:[0,1]
	v_and_b32_e32 v23, 0xffff0000, v15
	v_and_b32_e32 v27, 16, v15
	v_and_b32_e32 v26, 0xffff0000, v14
	v_lshlrev_b32_e32 v45, 16, v15
	v_lshlrev_b32_e32 v15, 16, v14
	v_mov_b32_e32 v14, v46
	v_pk_fma_f32 v[12:13], v[42:43], v[96:97], v[12:13] op_sel_hi:[1,0,1]
	v_pk_mov_b32 v[42:43], v[48:49], v[46:47] op_sel:[1,0]
	v_mov_b32_e32 v44, v26
	v_pk_mul_f32 v[42:43], v[98:99], v[42:43] op_sel_hi:[0,1]
	v_pk_mov_b32 v[26:27], v[14:15], v[26:27] op_sel:[1,0]
	v_mov_b32_e32 v22, v45
	v_pk_fma_f32 v[42:43], v[96:97], v[48:49], v[42:43] op_sel_hi:[0,1,1]
	v_pk_mul_f32 v[26:27], v[98:99], v[26:27] op_sel_hi:[0,1]
	s_waitcnt vmcnt(0)
	v_pk_fma_f32 v[42:43], v[100:101], v[14:15], v[42:43] op_sel_hi:[0,1,1]
	v_pk_fma_f32 v[14:15], v[96:97], v[14:15], v[26:27] op_sel_hi:[0,1,1]
	v_pk_mul_f32 v[26:27], v[98:99], v[22:23] op_sel_hi:[0,1]
	v_pk_fma_f32 v[26:27], v[96:97], v[44:45], v[26:27] op_sel_hi:[0,1,1]
	v_mov_b32_e32 v40, v23
	v_pk_fma_f32 v[12:13], v[100:101], v[48:49], v[12:13] op_sel_hi:[0,1,1]
	v_pk_fma_f32 v[14:15], v[100:101], v[44:45], v[14:15] op_sel_hi:[0,1,1]
	v_pk_fma_f32 v[22:23], v[100:101], v[40:41], v[26:27] op_sel_hi:[0,1,1]
	v_cvt_pk_bf16_f32 v12, v12, v13
	v_cvt_pk_bf16_f32 v13, v42, v43
	v_cvt_pk_bf16_f32 v14, v14, v15
	v_cvt_pk_bf16_f32 v15, v22, v23
	v_lshl_add_u32 v2, v59, 1, v19
	ds_write_b128 v2, v[12:15]
	v_ashrrev_i32_e32 v13, 10, v39
	v_lshlrev_b32_e32 v16, 9, v13
	v_add_u32_e32 v14, s46, v16
	v_ashrrev_i32_e32 v15, 31, v14
	v_lshl_add_u64 v[14:15], v[14:15], 2, s[4:5]
	v_add_u32_e32 v14, s11, v16
	v_ashrrev_i32_e32 v15, 31, v14
	v_lshl_add_u64 v[14:15], v[14:15], 2, s[4:5]
	v_add_u32_e32 v14, s10, v16
	v_ashrrev_i32_e32 v15, 31, v14
	v_lshl_add_u64 v[14:15], v[14:15], 2, s[4:5]
	v_cmp_lt_u32_e32 vcc, s23, v39
	s_and_saveexec_b64 s[0:1], vcc
	s_xor_b64 s[0:1], exec, s[0:1]
	s_cbranch_execz .LBB0_687
	s_mov_b64 s[38:39], src_shared_base
	s_cmp_lg_u32 0, -1
	s_cselect_b32 s38, 0, 0
	s_cselect_b32 s39, s39, 0
	s_add_u32 s38, s38, 0x1a1a0
	s_addc_u32 s39, s39, 0
	s_cmp_lg_u64 s[38:39], 0
	s_cselect_b32 s38, s38, -1
	s_add_i32 s39, 0, 0x1e1a0
	v_mov_b32_e32 v15, s39
	v_mov_b32_e32 v16, s38
	v_cmp_eq_u32_e32 vcc, 1, v13
	s_nop 1
	v_cndmask_b32_e32 v13, v15, v16, vcc
	v_lshl_add_u32 v63, v62, 13, v13
.LBB0_687:
	s_andn2_saveexec_b64 s[0:1], s[0:1]
	s_or_b64 exec, exec, s[0:1]
	v_lshlrev_b32_e32 v39, 16, v8
	v_and_b32_e32 v42, 0xffff0000, v8
	v_and_b32_e32 v40, 0xffff0000, v9
	v_lshlrev_b32_e32 v43, 16, v9
	v_mov_b32_e32 v8, v39
	v_mov_b32_e32 v9, v42
	v_and_b32_e32 v41, 16, v10
	s_waitcnt vmcnt(1)
	v_pk_mul_f32 v[8:9], v[104:105], v[8:9] op_sel_hi:[0,1]
	v_and_b32_e32 v19, 0xffff0000, v11
	v_and_b32_e32 v23, 16, v11
	v_and_b32_e32 v22, 0xffff0000, v10
	v_lshlrev_b32_e32 v27, 16, v11
	v_lshlrev_b32_e32 v11, 16, v10
	v_mov_b32_e32 v10, v40
	v_pk_fma_f32 v[8:9], v[38:39], v[102:103], v[8:9] op_sel_hi:[1,0,1]
	v_pk_mov_b32 v[38:39], v[42:43], v[40:41] op_sel:[1,0]
	v_mov_b32_e32 v26, v22
	v_mov_b32_e32 v18, v27
	v_pk_mul_f32 v[38:39], v[104:105], v[38:39] op_sel_hi:[0,1]
	v_pk_mov_b32 v[22:23], v[10:11], v[22:23] op_sel:[1,0]
	v_pk_fma_f32 v[38:39], v[102:103], v[42:43], v[38:39] op_sel_hi:[0,1,1]
	v_pk_mul_f32 v[22:23], v[104:105], v[22:23] op_sel_hi:[0,1]
	v_pk_mul_f32 v[12:13], v[104:105], v[18:19] op_sel_hi:[0,1]
	s_waitcnt vmcnt(0)
	v_pk_fma_f32 v[38:39], v[106:107], v[10:11], v[38:39] op_sel_hi:[0,1,1]
	v_pk_fma_f32 v[10:11], v[102:103], v[10:11], v[22:23] op_sel_hi:[0,1,1]
	v_pk_fma_f32 v[12:13], v[102:103], v[26:27], v[12:13] op_sel_hi:[0,1,1]
	v_mov_b32_e32 v36, v19
	v_pk_fma_f32 v[8:9], v[106:107], v[42:43], v[8:9] op_sel_hi:[0,1,1]
	v_pk_fma_f32 v[10:11], v[106:107], v[26:27], v[10:11] op_sel_hi:[0,1,1]
	v_pk_fma_f32 v[12:13], v[106:107], v[36:37], v[12:13] op_sel_hi:[0,1,1]
	v_cvt_pk_bf16_f32 v8, v8, v9
	v_cvt_pk_bf16_f32 v9, v38, v39
	v_cvt_pk_bf16_f32 v10, v10, v11
	v_cvt_pk_bf16_f32 v11, v12, v13
	v_lshl_add_u32 v2, v59, 1, v63
	ds_write_b128 v2, v[8:11]
	v_ashrrev_i32_e32 v9, 10, v35
	v_lshlrev_b32_e32 v12, 9, v9
	v_add_u32_e32 v10, s46, v12
	v_ashrrev_i32_e32 v11, 31, v10
	v_lshl_add_u64 v[10:11], v[10:11], 2, s[4:5]
	v_add_u32_e32 v10, s11, v12
	v_ashrrev_i32_e32 v11, 31, v10
	v_lshl_add_u64 v[10:11], v[10:11], 2, s[4:5]
	v_add_u32_e32 v10, s10, v12
	v_ashrrev_i32_e32 v11, 31, v10
	v_lshl_add_u64 v[10:11], v[10:11], 2, s[4:5]
	v_bfe_u32 v12, v35, 9, 1
	v_cmp_lt_u32_e32 vcc, s23, v35
	s_and_saveexec_b64 s[0:1], vcc
	s_xor_b64 s[0:1], exec, s[0:1]
	s_cbranch_execz .LBB0_689
	s_mov_b64 s[10:11], src_shared_base
	s_cmp_lg_u32 0, -1
	s_cselect_b32 s10, 0, 0
	s_cselect_b32 s11, s11, 0
	s_add_u32 s10, s10, 0x1a1a0
	s_addc_u32 s11, s11, 0
	s_cmp_lg_u64 s[10:11], 0
	s_cselect_b32 s10, s10, -1
	s_add_i32 s11, 0, 0x1e1a0
	v_mov_b32_e32 v11, s11
	v_mov_b32_e32 v13, s10
	v_cmp_eq_u32_e32 vcc, 1, v9
	s_nop 1
	v_cndmask_b32_e32 v9, v11, v13, vcc
	v_lshl_add_u32 v11, v12, 13, v9
.LBB0_689:
	s_andn2_saveexec_b64 s[0:1], s[0:1]
	v_mad_u32_u24 v11, v12, s24, v57
	s_or_b64 exec, exec, s[0:1]
	v_and_b32_e32 v23, 16, v6
	v_and_b32_e32 v22, 0xffff0000, v5
	v_and_b32_e32 v26, 0xffff0000, v4
	v_lshlrev_b32_e32 v27, 16, v5
	v_lshlrev_b32_e32 v35, 16, v4
	v_and_b32_e32 v13, 0xffff0000, v7
	v_and_b32_e32 v15, 16, v7
	v_and_b32_e32 v14, 0xffff0000, v6
	v_lshlrev_b32_e32 v19, 16, v7
	v_lshlrev_b32_e32 v7, 16, v6
	v_mov_b32_e32 v6, v22
	v_pk_mov_b32 v[22:23], v[26:27], v[22:23] op_sel:[1,0]
	v_mov_b32_e32 v18, v14
	v_mov_b32_e32 v12, v19
	v_mov_b32_e32 v4, v35
	v_mov_b32_e32 v5, v26
	s_waitcnt vmcnt(1)
	v_pk_mul_f32 v[22:23], v[104:105], v[22:23] op_sel_hi:[0,1]
	v_pk_mov_b32 v[14:15], v[6:7], v[14:15] op_sel:[1,0]
	s_mul_i32 s1, s46, 0x4400
	v_readlane_b32 s10, v251, 44
	v_pk_mul_f32 v[4:5], v[104:105], v[4:5] op_sel_hi:[0,1]
	v_pk_fma_f32 v[22:23], v[102:103], v[26:27], v[22:23] op_sel_hi:[0,1,1]
	v_pk_mul_f32 v[14:15], v[104:105], v[14:15] op_sel_hi:[0,1]
	v_pk_mul_f32 v[8:9], v[104:105], v[12:13] op_sel_hi:[0,1]
	s_mul_hi_i32 s0, s46, 0x4400
	v_readlane_b32 s11, v251, 45
	s_add_u32 s52, s10, s1
	v_pk_fma_f32 v[4:5], v[34:35], v[102:103], v[4:5] op_sel_hi:[1,0,1]
	s_waitcnt vmcnt(0)
	v_pk_fma_f32 v[22:23], v[106:107], v[6:7], v[22:23] op_sel_hi:[0,1,1]
	v_pk_fma_f32 v[6:7], v[102:103], v[6:7], v[14:15] op_sel_hi:[0,1,1]
	v_pk_fma_f32 v[8:9], v[102:103], v[18:19], v[8:9] op_sel_hi:[0,1,1]
	v_mov_b32_e32 v32, v13
	s_addc_u32 s53, s11, s0
	s_ashr_i32 s47, s48, 7
	s_lshr_b32 s0, s48, 1
	v_pk_fma_f32 v[4:5], v[106:107], v[26:27], v[4:5] op_sel_hi:[0,1,1]
	v_pk_fma_f32 v[6:7], v[106:107], v[18:19], v[6:7] op_sel_hi:[0,1,1]
	v_pk_fma_f32 v[8:9], v[106:107], v[32:33], v[8:9] op_sel_hi:[0,1,1]
	v_and_b32_e32 v2, 31, v1
	s_and_b32 s0, s0, 32
	s_mul_i32 s1, s47, 24
	v_cvt_pk_bf16_f32 v4, v4, v5
	v_cvt_pk_bf16_f32 v5, v22, v23
	v_cvt_pk_bf16_f32 v6, v6, v7
	v_cvt_pk_bf16_f32 v7, v8, v9
	v_lshl_add_u32 v9, v59, 1, v11
	v_or_b32_e32 v226, s0, v2
	s_add_i32 s1, s1, s0
	s_movk_i32 s10, 0x1806
	v_sub_u32_e32 v2, 0x1000, v2
	v_bfe_u32 v8, v1, 5, 1
	ds_write_b128 v9, v[4:7]
	s_sub_i32 s62, s1, 63
	v_cmp_gt_i32_e64 s[38:39], s10, v1
	v_and_b32_e32 v4, 3, v2
	s_movk_i32 s10, 0x4040
	v_and_b32_e32 v2, 0x1ffc, v2
	s_cmp_lt_i32 s47, 3
	v_mad_u32_u24 v4, v4, s10, 0
	v_lshlrev_b32_e32 v2, 1, v2
	v_lshlrev_b32_e32 v5, 4, v8
	s_cselect_b32 s63, 24, 23
	v_add3_u32 v2, v4, v2, v5
	s_lshl_b32 s10, s62, 7
	v_subrev_u32_e32 v228, s10, v2
	v_subrev_u32_e32 v2, s62, v226
	v_lshlrev_b32_e32 v4, 2, v1
	v_lshlrev_b32_e32 v6, 3, v8
	v_cmp_gt_u32_e64 s[40:41], 64, v2
	v_mul_lo_u32 v231, v2, s18
	v_lshlrev_b32_e32 v2, 4, v226
	v_and_b32_e32 v8, 0xffc, v4
	v_lshlrev_b32_e32 v182, 12, v56
	v_add3_u32 v2, 0, v2, v5
	v_mad_i32_i24 v4, v56, s22, 0
	v_and_b32_e32 v5, 0x3f0, v1
	v_lshlrev_b32_e32 v9, 2, v8
	v_ashrrev_i32_e32 v183, 31, v182
	v_add3_u32 v239, v4, v5, v9
	v_lshl_add_u64 v[4:5], v[182:183], 1, s[52:53]
	v_lshlrev_b32_e32 v184, 1, v8
	v_mov_b32_e32 v185, v3
	v_and_b32_e32 v10, 0x3f8, v1
	v_lshl_add_u64 v[186:187], v[4:5], 0, v[184:185]
	v_lshlrev_b32_e32 v4, 2, v58
	v_mul_i32_i24_e32 v9, 0x1400, v56
	v_add_u32_e32 v11, v8, v10
	v_and_b32_e32 v8, 0xffc, v4
	v_lshlrev_b32_e32 v183, 1, v9
	v_mad_i32_i24 v4, v25, s22, 0
	v_and_b32_e32 v5, 0x3f0, v58
	v_lshlrev_b32_e32 v9, 2, v8
	v_lshlrev_b32_e32 v188, 12, v25
	v_add3_u32 v241, v4, v5, v9
	v_and_b32_e32 v4, 0x3f8, v58
	v_ashrrev_i32_e32 v189, 31, v188
	v_lshlrev_b32_e32 v185, 1, v11
	v_add_u32_e32 v11, v8, v4
	v_lshl_add_u64 v[4:5], v[188:189], 1, s[52:53]
	v_lshlrev_b32_e32 v190, 1, v8
	v_mov_b32_e32 v191, v3
	v_lshl_add_u64 v[192:193], v[4:5], 0, v[190:191]
	v_lshlrev_b32_e32 v4, 2, v60
	v_mul_i32_i24_e32 v9, 0x1400, v25
	v_and_b32_e32 v8, 0xffc, v4
	v_lshlrev_b32_e32 v194, 12, v21
	v_lshlrev_b32_e32 v189, 1, v9
	v_mad_i32_i24 v4, v21, s22, 0
	v_and_b32_e32 v5, 0x3f0, v60
	v_lshlrev_b32_e32 v9, 2, v8
	v_ashrrev_i32_e32 v195, 31, v194
	s_add_i32 s64, s63, -1
	v_add3_u32 v243, v4, v5, v9
	v_lshl_add_u64 v[4:5], v[194:195], 1, s[52:53]
	v_lshlrev_b32_e32 v196, 1, v8
	v_mov_b32_e32 v197, v3
	s_cmpk_gt_u32 s48, 0x7f
	v_lshl_add_u64 v[198:199], v[4:5], 0, v[196:197]
	v_lshlrev_b32_e32 v4, 2, v61
	s_cselect_b64 s[48:49], -1, 0
	v_mul_i32_i24_e32 v9, 0x1400, v21
	v_add_u32_e32 v10, v8, v10
	v_and_b32_e32 v8, 0xffc, v4
	s_add_i32 s65, s46, s12
	v_lshlrev_b32_e32 v195, 1, v9
	v_mad_i32_i24 v4, v17, s22, 0
	v_and_b32_e32 v5, 0x3f0, v61
	v_lshlrev_b32_e32 v9, 2, v8
	v_lshlrev_b32_e32 v200, 12, v17
	s_add_u32 s10, s60, s44
	v_add3_u32 v245, v4, v5, v9
	v_and_b32_e32 v4, 0x3f8, v61
	v_ashrrev_i32_e32 v201, 31, v200
	s_addc_u32 s11, s61, s45
	v_lshlrev_b32_e32 v197, 1, v10
	v_mul_i32_i24_e32 v9, 0x1400, v17
	v_add_u32_e32 v10, v8, v4
	v_lshl_add_u64 v[4:5], v[200:201], 1, s[52:53]
	v_lshlrev_b32_e32 v202, 1, v8
	v_mov_b32_e32 v203, v3
	s_add_u32 s10, s10, 0x1050000
	v_lshlrev_b32_e32 v7, 8, v226
	v_lshlrev_b32_e32 v191, 1, v11
	v_lshl_add_u64 v[204:205], v[4:5], 0, v[202:203]
	v_lshlrev_b32_e32 v201, 1, v9
	v_lshlrev_b32_e32 v203, 1, v10
	s_addc_u32 s11, s11, 0
	v_lshl_add_u32 v227, v28, 1, 0
	v_cmp_gt_i32_e64 s[0:1], 4, v1
	v_add_u32_e32 v229, 0x48, v228
	v_add_u32_e32 v230, 0x68, v228
	v_subrev_u32_e32 v232, 64, v228
	v_subrev_u32_e32 v233, 56, v228
	v_subrev_u32_e32 v234, 32, v228
	v_subrev_u32_e32 v235, 24, v228
	v_add_u32_e32 v236, 8, v228
	v_add_u32_e32 v237, 40, v228
	v_add_u32_e32 v238, 0, v28
	v_add3_u32 v240, s19, v183, v185
	v_add3_u32 v242, s19, v189, v191
	v_add3_u32 v244, s19, v195, v197
	v_add3_u32 v246, s19, v201, v203
	v_lshl_add_u64 v[206:207], v[28:29], 1, s[10:11]
	v_lshl_add_u64 v[208:209], v[30:31], 1, s[10:11]
	s_mov_b32 s42, 0
	s_mov_b64 s[44:45], -1
	v_lshlrev_b32_e32 v247, 1, v6
	v_add_u32_e32 v212, v2, v7
	s_branch .LBB0_693

	.amdhsa_kernel _ZN2mk4megaENS_4ArgsE
		.amdhsa_group_segment_fixed_size 0
		.amdhsa_private_segment_fixed_size 0
		.amdhsa_kernarg_size 552
		.amdhsa_user_sgpr_count 2
		.amdhsa_user_sgpr_dispatch_ptr 0
		.amdhsa_user_sgpr_queue_ptr 0
		.amdhsa_user_sgpr_kernarg_segment_ptr 1
		.amdhsa_user_sgpr_dispatch_id 0
		.amdhsa_user_sgpr_kernarg_preload_length 0
		.amdhsa_user_sgpr_kernarg_preload_offset 0
		.amdhsa_user_sgpr_private_segment_size 0
		.amdhsa_uses_dynamic_stack 0
		.amdhsa_enable_private_segment 0
		.amdhsa_system_sgpr_workgroup_id_x 1
		.amdhsa_system_sgpr_workgroup_id_y 0
		.amdhsa_system_sgpr_workgroup_id_z 0
		.amdhsa_system_sgpr_workgroup_info 0
		.amdhsa_system_vgpr_workitem_id 0
		.amdhsa_next_free_vgpr 256
		.amdhsa_next_free_sgpr 102
		.amdhsa_accum_offset 256
		.amdhsa_reserve_vcc 1
		.amdhsa_float_round_mode_32 0
		.amdhsa_float_round_mode_16_64 0
		.amdhsa_float_denorm_mode_32 3
		.amdhsa_float_denorm_mode_16_64 3
		.amdhsa_dx10_clamp 1
		.amdhsa_ieee_mode 1
		.amdhsa_fp16_overflow 0
		.amdhsa_tg_split 0
		.amdhsa_exception_fp_ieee_invalid_op 0
		.amdhsa_exception_fp_denorm_src 0
		.amdhsa_exception_fp_ieee_div_zero 0
		.amdhsa_exception_fp_ieee_overflow 0
		.amdhsa_exception_fp_ieee_underflow 0
		.amdhsa_exception_fp_ieee_inexact 0
		.amdhsa_exception_int_div_zero 0
	.end_amdhsa_kernel

amdhsa.kernels:
  - .agpr_count:     0
    .args:
      - .offset:         0
        .size:           296
        .value_kind:     by_value
      - .offset:         296
        .size:           4
        .value_kind:     hidden_block_count_x
      - .offset:         300
        .size:           4
        .value_kind:     hidden_block_count_y
      - .offset:         304
        .size:           4
        .value_kind:     hidden_block_count_z
      - .offset:         308
        .size:           2
        .value_kind:     hidden_group_size_x
      - .offset:         310
        .size:           2
        .value_kind:     hidden_group_size_y
      - .offset:         312
        .size:           2
        .value_kind:     hidden_group_size_z
      - .offset:         314
        .size:           2
        .value_kind:     hidden_remainder_x
      - .offset:         316
        .size:           2
        .value_kind:     hidden_remainder_y
      - .offset:         318
        .size:           2
        .value_kind:     hidden_remainder_z
      - .offset:         336
        .size:           8
        .value_kind:     hidden_global_offset_x
      - .offset:         344
        .size:           8
        .value_kind:     hidden_global_offset_y
      - .offset:         352
        .size:           8
        .value_kind:     hidden_global_offset_z
      - .offset:         360
        .size:           2
        .value_kind:     hidden_grid_dims
      - .offset:         416
        .size:           4
        .value_kind:     hidden_dynamic_lds_size
    .group_segment_fixed_size: 0
    .kernarg_segment_align: 8
    .kernarg_segment_size: 552
    .language:       OpenCL C
    .language_version:
      - 2
      - 0
    .max_flat_workgroup_size: 512
    .name:           _ZN2mk4megaENS_4ArgsE
    .private_segment_fixed_size: 0
    .sgpr_count:     108
    .sgpr_spill_count: 569
    .symbol:         _ZN2mk4megaENS_4ArgsE.kd
    .uniform_work_group_size: 1
    .uses_dynamic_stack: false
    .vgpr_count:     256
    .vgpr_spill_count: 0
    .wavefront_size: 64
